# mLSTM pass-2 chunk tail: the normaliser dot-product loop issues its ten LDS reads together with counted waits instead of one read and a full LDS wait per term (same accumulation order)
# speedup vs baseline: 1.0054x; 1.0054x over previous
; #define LAS __attribute__((address_space(3)))
; DI float bf2f(unsigned short s) { return __uint_as_float(((unsigned)s) << 16); }
; template <bool PASS2, int DIRT>
; DI void mlstm_item(const Params& P, LAS unsigned char* lds, int st, int g) {
;     ...
;         { const int dk = tid & 127, part = tid >> 7; float s = 0.f;
; #pragma unroll 8
;           for (int i = 0; i < 32; ++i) { const int sp = 32 * part + i; s += sEV[sp] * bf2f(*(const LAS unsigned short*)(KS + off_b(sp, dk >> 3) + (dk & 7) * 2)); }
;           sNPART[part * 128 + dk] = s; }
;         __syncthreads();
;         if (tid < 128) sN0[tid] = a * sN0[tid] + ((sNPART[tid] + sNPART[128 + tid]) + (sNPART[256 + tid] + sNPART[384 + tid]));
.LBB0_762:
	v_add_u32_e32 v67, 0, v66
	v_add_u32_e32 v68, 0x1a000, v67
	v_add_u32_e32 v72, 0, v65
	v_add_u32_e32 v67, 0x1a010, v67
	ds_read_b128 v[68:71], v68
	ds_read_u16 v73, v72
	ds_read_u16 v244, v72 offset:272
	ds_read_u16 v245, v72 offset:544
	ds_read_u16 v246, v72 offset:816
	ds_read_b128 v[74:77], v67
	ds_read_u16 v247, v72 offset:1088
	ds_read_u16 v248, v72 offset:1360
	ds_read_u16 v249, v72 offset:1632
	ds_read_u16 v250, v72 offset:1904
	s_add_i32 s2, s2, -8
	v_add_u32_e32 v65, 0x880, v65
	v_add_u32_e32 v66, 32, v66
	s_cmp_eq_u32 s2, 0
	s_waitcnt lgkmcnt(8)
	v_lshlrev_b32_e32 v73, 16, v73
	v_fmac_f32_e32 v64, v68, v73
	s_waitcnt lgkmcnt(7)
	v_lshlrev_b32_e32 v244, 16, v244
	v_fmac_f32_e32 v64, v69, v244
	s_waitcnt lgkmcnt(6)
	v_lshlrev_b32_e32 v245, 16, v245
	v_fmac_f32_e32 v64, v70, v245
	s_waitcnt lgkmcnt(5)
	v_lshlrev_b32_e32 v246, 16, v246
	v_fmac_f32_e32 v64, v71, v246
	s_waitcnt lgkmcnt(3)
	v_lshlrev_b32_e32 v247, 16, v247
	v_fmac_f32_e32 v64, v74, v247
	s_waitcnt lgkmcnt(2)
	v_lshlrev_b32_e32 v248, 16, v248
	v_fmac_f32_e32 v64, v75, v248
	s_waitcnt lgkmcnt(1)
	v_lshlrev_b32_e32 v249, 16, v249
	v_fmac_f32_e32 v64, v76, v249
	s_waitcnt lgkmcnt(0)
	v_lshlrev_b32_e32 v250, 16, v250
	v_fmac_f32_e32 v64, v77, v250
	s_cbranch_scc0 .LBB0_762
	v_lshl_add_u32 v65, v97, 2, 0
	v_add_u32_e32 v66, 0x1b800, v65
	v_cmp_gt_i32_e32 vcc, s63, v97
	ds_write_b32 v66, v64
	s_waitcnt lgkmcnt(0)
	s_barrier
	s_and_saveexec_b64 s[2:3], vcc
	s_cbranch_execz .LBB0_737
	ds_read2st64_b32 v[68:69], v66 offset1:2
	ds_read2st64_b32 v[66:67], v66 offset0:4 offset1:6
	v_add_u32_e32 v70, 0x1a600, v65
	ds_read_b32 v71, v70
	s_waitcnt lgkmcnt(2)
	v_mov_b32_e32 v64, v68
	s_waitcnt lgkmcnt(1)
	v_mov_b32_e32 v65, v66
	v_mov_b32_e32 v66, v69
	v_pk_add_f32 v[64:65], v[64:65], v[66:67]
	s_nop 0
	v_add_f32_e32 v64, v64, v65
	s_waitcnt lgkmcnt(0)
	v_fmac_f32_e32 v64, v96, v71
	ds_write_b32 v70, v64
	s_branch .LBB0_737
